# stack22 = stack19 + second down-projection loop: last trip peeled without its unused weight requests + router-logit loops: unused last-trip weight requests skipped (the code behind waited for them)
# speedup vs baseline: 1.0069x; 1.0069x over previous
; DEVINL void phase4(const Params& P, unsigned char* smem) {
;     ...
;             for (int p = 0; p < 4; ++p) {
;                 union { bf16x8 v; unsigned u[4]; } hh[2], hl[2];
;                 unsigned h8[2][2];
; #pragma unroll
;                 for (int q = 0; q < 2; ++q) {
;                     const int nt = 2 * p + q, col = 128 * wv + 16 * nt + 4 * g;
;                     const f32x4 mul = *(const f32x4*)(s_t2 + col), sh = *(const f32x4*)(s_t3 + col);
; #pragma unroll
;                     for (int mi2 = 0; mi2 < 2; ++mi2) {
;                         const f32x4 h = xl[(nt * 2 + mi2) * 512] * rt2[mi2] * mul + sh;
;                         const unsigned u01 = pk2(h.x, h.y), u23 = pk2(h.z, h.w);
;                         hh[mi2].u[2 * q] = u01; hh[mi2].u[2 * q + 1] = u23;
;                         hl[mi2].u[2 * q] = pk2(h.x - bflo(u01), h.y - bfhi(u01));
;                         hl[mi2].u[2 * q + 1] = pk2(h.z - bflo(u23), h.w - bfhi(u23));
;                         h8[q][mi2] = pk4_fp8(h.x, h.y, h.z, h.w);
;                     }
;                 }
;                 __builtin_amdgcn_sched_barrier(0);
; #pragma unroll
;                 for (int ot = 0; ot < 3; ++ot) {
;                     const bf16x8 whi = rwh[ot], wlo = rwl[ot];
; #pragma unroll
;                     for (int mi2 = 0; mi2 < 2; ++mi2) {
;                         f32x4 a = lg[ot][2 * hf + mi2];
;                         a = __builtin_amdgcn_mfma_f32_16x16x32_bf16(whi, hh[mi2].v, a, 0, 0, 0);
;                         a = __builtin_amdgcn_mfma_f32_16x16x32_bf16(whi, hl[mi2].v, a, 0, 0, 0);
;                         a = __builtin_amdgcn_mfma_f32_16x16x32_bf16(wlo, hh[mi2].v, a, 0, 0, 0);
;                         lg[ot][2 * hf + mi2] = a;
;                     }
;                 }
;                 __builtin_amdgcn_sched_barrier(0);
;                 { const int pn = p < 3 ? p + 1 : 3;
; #pragma unroll
;                   for (int ot = 0; ot < 3; ++ot) { rwh[ot] = *(const bf16x8*)(wr + (size_t)(pn * 3 + ot) * 512); rwl[ot] = *(const bf16x8*)(wr + (size_t)(4 * 8 * 3 * 64) * 8 + (size_t)(pn * 3 + ot) * 512); } }
;                 __builtin_amdgcn_sched_barrier(0);
; #pragma unroll
;                 for (int mi2 = 0; mi2 < 2; ++mi2) {
;                     const auto rr = __builtin_amdgcn_permlane16_swap(h8[0][mi2], h8[1][mi2], false, false);
.LBB0_596:
	v_add_u32_e32 v215, s0, v135
	v_add_u32_e32 v114, 0x22000, v215
	ds_read_b128 v[120:123], v114
	v_add_u32_e32 v114, 0x23000, v215
	ds_read_b128 v[124:127], v114
	ds_read_b128 v[114:117], v245
	ds_read_b128 v[226:229], v245 offset:8192
	v_mov_b32_e32 v214, 0
	s_waitcnt lgkmcnt(1)
	v_pk_mul_f32 v[116:117], v[204:205], v[116:117]
	v_pk_mul_f32 v[114:115], v[190:191], v[114:115]
	v_pk_fma_f32 v[116:117], v[122:123], v[116:117], v[126:127]
	v_pk_fma_f32 v[128:129], v[120:121], v[114:115], v[124:125]
	v_cvt_pk_bf16_f32 v115, v116, v117
	v_cvt_pk_bf16_f32 v114, v128, v129
	v_lshlrev_b32_e32 v118, 16, v114
	v_and_b32_e32 v119, 0xffff0000, v114
	v_lshlrev_b32_e32 v212, 16, v115
	v_and_b32_e32 v213, 0xffff0000, v115
	v_pk_add_f32 v[118:119], v[128:129], v[118:119] neg_lo:[0,1] neg_hi:[0,1]
	v_pk_add_f32 v[212:213], v[116:117], v[212:213] neg_lo:[0,1] neg_hi:[0,1]
	v_cvt_pk_bf16_f32 v118, v118, v119
	v_cvt_pk_bf16_f32 v119, v212, v213
	v_mov_b32_e32 v212, 0
	v_cvt_pk_fp8_f32 v212, v128, v129
	s_waitcnt lgkmcnt(0)
	v_pk_mul_f32 v[128:129], v[202:203], v[226:227]
	v_mov_b32_e32 v213, 0
	v_pk_fma_f32 v[120:121], v[120:121], v[128:129], v[124:125]
	v_cvt_pk_fp8_f32 v212, v116, v117 op_sel:[0,0,1]
	v_pk_mul_f32 v[116:117], v[206:207], v[228:229]
	v_cvt_pk_fp8_f32 v214, v120, v121
	v_pk_fma_f32 v[116:117], v[122:123], v[116:117], v[126:127]
	v_cvt_pk_bf16_f32 v122, v120, v121
	v_lshlrev_b32_e32 v124, 16, v122
	v_and_b32_e32 v125, 0xffff0000, v122
	v_cvt_pk_bf16_f32 v123, v116, v117
	v_pk_add_f32 v[124:125], v[120:121], v[124:125] neg_lo:[0,1] neg_hi:[0,1]
	v_cvt_pk_fp8_f32 v214, v116, v117 op_sel:[0,0,1]
	v_cvt_pk_bf16_f32 v126, v124, v125
	v_lshlrev_b32_e32 v124, 16, v123
	v_and_b32_e32 v125, 0xffff0000, v123
	v_pk_add_f32 v[124:125], v[116:117], v[124:125] neg_lo:[0,1] neg_hi:[0,1]
	v_add_u32_e32 v116, 0x22040, v215
	ds_read_b128 v[226:229], v116
	v_add_u32_e32 v116, 0x23040, v215
	ds_read_b128 v[230:233], v116
	ds_read_b128 v[234:237], v245 offset:16384
	v_cvt_pk_bf16_f32 v127, v124, v125
	v_mov_b32_e32 v215, 0
	s_waitcnt lgkmcnt(0)
	v_pk_mul_f32 v[116:117], v[204:205], v[236:237]
	v_pk_mul_f32 v[120:121], v[190:191], v[234:235]
	v_pk_fma_f32 v[124:125], v[228:229], v[116:117], v[232:233]
	v_pk_fma_f32 v[128:129], v[226:227], v[120:121], v[230:231]
	v_cvt_pk_bf16_f32 v117, v124, v125
	v_cvt_pk_bf16_f32 v116, v128, v129
	v_lshlrev_b32_e32 v120, 16, v116
	v_and_b32_e32 v121, 0xffff0000, v116
	v_lshlrev_b32_e32 v234, 16, v117
	v_and_b32_e32 v235, 0xffff0000, v117
	v_pk_add_f32 v[120:121], v[128:129], v[120:121] neg_lo:[0,1] neg_hi:[0,1]
	v_pk_add_f32 v[234:235], v[124:125], v[234:235] neg_lo:[0,1] neg_hi:[0,1]
	v_cvt_pk_bf16_f32 v120, v120, v121
	v_cvt_pk_bf16_f32 v121, v234, v235
	ds_read_b128 v[234:237], v245 offset:24576
	v_cvt_pk_fp8_f32 v213, v128, v129
	s_waitcnt lgkmcnt(0)
	v_pk_mul_f32 v[128:129], v[202:203], v[234:235]
	v_cvt_pk_fp8_f32 v213, v124, v125 op_sel:[0,0,1]
	v_pk_mul_f32 v[124:125], v[206:207], v[236:237]
	v_pk_fma_f32 v[226:227], v[226:227], v[128:129], v[230:231]
	v_pk_fma_f32 v[228:229], v[228:229], v[124:125], v[232:233]
	v_cvt_pk_fp8_f32 v215, v226, v227
	v_cvt_pk_bf16_f32 v124, v226, v227
	v_cvt_pk_bf16_f32 v125, v228, v229
	v_lshlrev_b32_e32 v128, 16, v124
	v_and_b32_e32 v129, 0xffff0000, v124
	v_lshlrev_b32_e32 v230, 16, v125
	v_and_b32_e32 v231, 0xffff0000, v125
	v_pk_add_f32 v[128:129], v[226:227], v[128:129] neg_lo:[0,1] neg_hi:[0,1]
	v_pk_add_f32 v[230:231], v[228:229], v[230:231] neg_lo:[0,1] neg_hi:[0,1]
	v_cvt_pk_bf16_f32 v128, v128, v129
	v_cvt_pk_bf16_f32 v129, v230, v231
	v_cvt_pk_fp8_f32 v215, v228, v229 op_sel:[0,0,1]
	s_waitcnt vmcnt(5)
	v_mfma_f32_16x16x32_bf16 v[82:85], v[94:97], v[114:117], v[82:85]
	v_mfma_f32_16x16x32_bf16 v[86:89], v[94:97], v[122:125], v[86:89]
	s_waitcnt vmcnt(4)
	v_mfma_f32_16x16x32_bf16 v[78:81], v[90:93], v[114:117], v[78:81]
	v_mfma_f32_16x16x32_bf16 v[74:77], v[90:93], v[122:125], v[74:77]
	s_waitcnt vmcnt(2)
	v_mfma_f32_16x16x32_bf16 v[70:73], v[98:101], v[114:117], v[70:73]
	v_mfma_f32_16x16x32_bf16 v[66:69], v[98:101], v[122:125], v[66:69]
	v_mfma_f32_16x16x32_bf16 v[82:85], v[94:97], v[118:121], v[82:85]
	v_mfma_f32_16x16x32_bf16 v[86:89], v[94:97], v[126:129], v[86:89]
	v_mfma_f32_16x16x32_bf16 v[78:81], v[90:93], v[118:121], v[78:81]
	v_mfma_f32_16x16x32_bf16 v[74:77], v[90:93], v[126:129], v[74:77]
	v_mfma_f32_16x16x32_bf16 v[70:73], v[98:101], v[118:121], v[70:73]
	v_mfma_f32_16x16x32_bf16 v[66:69], v[98:101], v[126:129], v[66:69]
	v_mfma_f32_16x16x32_bf16 v[82:85], v[106:109], v[114:117], v[82:85]
	v_mfma_f32_16x16x32_bf16 v[86:89], v[106:109], v[122:125], v[86:89]
	s_waitcnt vmcnt(1)
	v_mfma_f32_16x16x32_bf16 v[78:81], v[110:113], v[114:117], v[78:81]
	v_mfma_f32_16x16x32_bf16 v[74:77], v[110:113], v[122:125], v[74:77]
	s_waitcnt vmcnt(0)
	v_mfma_f32_16x16x32_bf16 v[70:73], v[102:105], v[114:117], v[70:73]
	v_mfma_f32_16x16x32_bf16 v[66:69], v[102:105], v[122:125], v[66:69]
	s_cmpk_eq_i32 s0, 0x180
	s_cbranch_scc1 .Lrt_skip0
	s_cmpk_lg_i32 s0, 0x180
	s_cselect_b32 s24, s1, 0x1200
	s_lshl_b64 s[14:15], s[24:25], 1
	v_lshl_add_u64 v[98:99], v[130:131], 0, s[14:15]
	v_lshl_add_u64 v[100:101], v[132:133], 0, s[14:15]
	s_add_i32 s14, s24, 0x200
	s_mov_b32 s15, s25
	s_addk_i32 s24, 0x400
	v_lshl_add_u64 v[102:103], s[14:15], 1, v[132:133]
	v_lshl_add_u64 v[104:105], s[24:25], 1, v[132:133]
	global_load_dwordx4 v[94:97], v[98:99], off
	global_load_dwordx4 v[90:93], v[98:99], off offset:1024
	global_load_dwordx4 v[106:109], v[100:101], off
	s_nop 0
	global_load_dwordx4 v[98:101], v[98:99], off offset:2048
	s_nop 0
	global_load_dwordx4 v[110:113], v[102:103], off
	s_nop 0
	global_load_dwordx4 v[102:105], v[104:105], off
.Lrt_skip0:
	v_permlane16_swap_b32_e32 v212, v213
	v_permlane16_swap_b32_e32 v214, v215
	global_store_dwordx2 v[208:209], v[212:213], off
	global_store_dwordx2 v[210:211], v[214:215], off
	s_addk_i32 s1, 0x600
	s_addk_i32 s0, 0x80
	v_add_u32_e32 v245, 0x8000, v245
	v_lshl_add_u64 v[208:209], v[208:209], 0, 32
	s_cmpk_lg_i32 s0, 0x200
	v_lshl_add_u64 v[210:211], v[210:211], 0, 32
	s_cbranch_scc1 .LBB0_596

; DEVINL void phase4(const Params& P, unsigned char* smem) {
;     ...
;             for (int p = 0; p < 4; ++p) {
;                 union { bf16x8 v; unsigned u[4]; } hh[2], hl[2];
;                 unsigned h8[2][2];
; #pragma unroll
;                 for (int q = 0; q < 2; ++q) {
;                     const int nt = 2 * p + q, col = 128 * wv + 16 * nt + 4 * g;
;                     const f32x4 mul = *(const f32x4*)(s_t2 + col), sh = *(const f32x4*)(s_t3 + col);
; #pragma unroll
;                     for (int mi2 = 0; mi2 < 2; ++mi2) {
;                         const f32x4 h = xl[(nt * 2 + mi2) * 512] * rt2[mi2] * mul + sh;
;                         const unsigned u01 = pk2(h.x, h.y), u23 = pk2(h.z, h.w);
;                         hh[mi2].u[2 * q] = u01; hh[mi2].u[2 * q + 1] = u23;
;                         hl[mi2].u[2 * q] = pk2(h.x - bflo(u01), h.y - bfhi(u01));
;                         hl[mi2].u[2 * q + 1] = pk2(h.z - bflo(u23), h.w - bfhi(u23));
;                         h8[q][mi2] = pk4_fp8(h.x, h.y, h.z, h.w);
;                     }
;                 }
;                 __builtin_amdgcn_sched_barrier(0);
; #pragma unroll
;                 for (int ot = 0; ot < 3; ++ot) {
;                     const bf16x8 whi = rwh[ot], wlo = rwl[ot];
; #pragma unroll
;                     for (int mi2 = 0; mi2 < 2; ++mi2) {
;                         f32x4 a = lg[ot][2 * hf + mi2];
;                         a = __builtin_amdgcn_mfma_f32_16x16x32_bf16(whi, hh[mi2].v, a, 0, 0, 0);
;                         a = __builtin_amdgcn_mfma_f32_16x16x32_bf16(whi, hl[mi2].v, a, 0, 0, 0);
;                         a = __builtin_amdgcn_mfma_f32_16x16x32_bf16(wlo, hh[mi2].v, a, 0, 0, 0);
;                         lg[ot][2 * hf + mi2] = a;
;                     }
;                 }
;                 __builtin_amdgcn_sched_barrier(0);
;                 { const int pn = p < 3 ? p + 1 : 3;
; #pragma unroll
;                   for (int ot = 0; ot < 3; ++ot) { rwh[ot] = *(const bf16x8*)(wr + (size_t)(pn * 3 + ot) * 512); rwl[ot] = *(const bf16x8*)(wr + (size_t)(4 * 8 * 3 * 64) * 8 + (size_t)(pn * 3 + ot) * 512); } }
;                 __builtin_amdgcn_sched_barrier(0);
; #pragma unroll
;                 for (int mi2 = 0; mi2 < 2; ++mi2) {
;                     const auto rr = __builtin_amdgcn_permlane16_swap(h8[0][mi2], h8[1][mi2], false, false);
.LBB0_603:
	v_add_u32_e32 v63, s0, v135
	v_add_u32_e32 v64, 0x22000, v63
	v_add_u32_e32 v65, 0x23000, v63
	ds_read_b128 v[90:93], v62
	ds_read_b128 v[94:97], v64
	s_waitcnt vmcnt(10)
	ds_read_b128 v[98:101], v65
	s_waitcnt vmcnt(8)
	ds_read_b128 v[102:105], v62 offset:8192
	v_mov_b32_e32 v122, 0
	s_waitcnt lgkmcnt(3)
	v_pk_mul_f32 v[64:65], v[54:55], v[92:93]
	v_pk_mul_f32 v[90:91], v[50:51], v[90:91]
	s_waitcnt lgkmcnt(1)
	v_pk_fma_f32 v[64:65], v[96:97], v[64:65], v[100:101]
	v_pk_fma_f32 v[92:93], v[94:95], v[90:91], v[98:99]
	v_cvt_pk_bf16_f32 v91, v64, v65
	v_cvt_pk_bf16_f32 v90, v92, v93
	v_lshlrev_b32_e32 v106, 16, v90
	v_and_b32_e32 v107, 0xffff0000, v90
	v_lshlrev_b32_e32 v108, 16, v91
	v_cvt_pk_fp8_f32 v122, v92, v93
	v_and_b32_e32 v109, 0xffff0000, v91
	v_pk_add_f32 v[106:107], v[92:93], v[106:107] neg_lo:[0,1] neg_hi:[0,1]
	v_pk_add_f32 v[92:93], v[64:65], v[108:109] neg_lo:[0,1] neg_hi:[0,1]
	v_cvt_pk_bf16_f32 v106, v106, v107
	v_cvt_pk_bf16_f32 v107, v92, v93
	s_waitcnt lgkmcnt(0)
	v_pk_mul_f32 v[92:93], v[52:53], v[102:103]
	v_cvt_pk_fp8_f32 v122, v64, v65 op_sel:[0,0,1]
	v_pk_fma_f32 v[92:93], v[94:95], v[92:93], v[98:99]
	v_pk_mul_f32 v[64:65], v[56:57], v[104:105]
	v_cvt_pk_bf16_f32 v94, v92, v93
	v_pk_fma_f32 v[64:65], v[96:97], v[64:65], v[100:101]
	v_lshlrev_b32_e32 v96, 16, v94
	v_and_b32_e32 v97, 0xffff0000, v94
	v_mov_b32_e32 v104, 0
	v_pk_add_f32 v[96:97], v[92:93], v[96:97] neg_lo:[0,1] neg_hi:[0,1]
	v_cvt_pk_fp8_f32 v104, v92, v93
	v_add_u32_e32 v92, 0x22040, v63
	v_add_u32_e32 v63, 0x23040, v63
	ds_read_b128 v[100:103], v62 offset:16384
	ds_read_b128 v[110:113], v92
	ds_read_b128 v[114:117], v63
	v_cvt_pk_bf16_f32 v95, v64, v65
	v_cvt_pk_bf16_f32 v98, v96, v97
	v_lshlrev_b32_e32 v96, 16, v95
	v_and_b32_e32 v97, 0xffff0000, v95
	v_pk_add_f32 v[96:97], v[64:65], v[96:97] neg_lo:[0,1] neg_hi:[0,1]
	s_waitcnt lgkmcnt(2)
	v_pk_mul_f32 v[92:93], v[50:51], v[100:101]
	v_cvt_pk_bf16_f32 v99, v96, v97
	s_waitcnt lgkmcnt(0)
	v_pk_fma_f32 v[96:97], v[110:111], v[92:93], v[114:115]
	v_cvt_pk_fp8_f32 v104, v64, v65 op_sel:[0,0,1]
	ds_read_b128 v[118:121], v62 offset:24576
	v_pk_mul_f32 v[64:65], v[54:55], v[102:103]
	v_cvt_pk_bf16_f32 v92, v96, v97
	v_pk_fma_f32 v[64:65], v[112:113], v[64:65], v[116:117]
	v_lshlrev_b32_e32 v100, 16, v92
	v_and_b32_e32 v101, 0xffff0000, v92
	v_cvt_pk_bf16_f32 v93, v64, v65
	v_pk_add_f32 v[100:101], v[96:97], v[100:101] neg_lo:[0,1] neg_hi:[0,1]
	v_mov_b32_e32 v123, 0
	v_cvt_pk_bf16_f32 v108, v100, v101
	v_lshlrev_b32_e32 v100, 16, v93
	v_cvt_pk_fp8_f32 v123, v96, v97
	v_and_b32_e32 v101, 0xffff0000, v93
	v_pk_add_f32 v[96:97], v[64:65], v[100:101] neg_lo:[0,1] neg_hi:[0,1]
	v_mov_b32_e32 v105, 0
	v_cvt_pk_bf16_f32 v109, v96, v97
	s_waitcnt lgkmcnt(0)
	v_pk_mul_f32 v[96:97], v[52:53], v[118:119]
	v_cvt_pk_fp8_f32 v123, v64, v65 op_sel:[0,0,1]
	v_pk_fma_f32 v[100:101], v[110:111], v[96:97], v[114:115]
	v_pk_mul_f32 v[64:65], v[56:57], v[120:121]
	v_cvt_pk_fp8_f32 v105, v100, v101
	v_pk_fma_f32 v[64:65], v[112:113], v[64:65], v[116:117]
	v_cvt_pk_bf16_f32 v96, v100, v101
	v_cvt_pk_bf16_f32 v97, v64, v65
	v_lshlrev_b32_e32 v102, 16, v96
	v_and_b32_e32 v103, 0xffff0000, v96
	v_pk_add_f32 v[100:101], v[100:101], v[102:103] neg_lo:[0,1] neg_hi:[0,1]
	v_lshlrev_b32_e32 v102, 16, v97
	v_and_b32_e32 v103, 0xffff0000, v97
	v_cvt_pk_fp8_f32 v105, v64, v65 op_sel:[0,0,1]
	v_pk_add_f32 v[64:65], v[64:65], v[102:103] neg_lo:[0,1] neg_hi:[0,1]
	v_cvt_pk_bf16_f32 v100, v100, v101
	v_cvt_pk_bf16_f32 v101, v64, v65
	s_waitcnt vmcnt(5)
	v_mfma_f32_16x16x32_bf16 v[18:21], v[30:33], v[90:93], v[18:21]
	v_mfma_f32_16x16x32_bf16 v[22:25], v[30:33], v[94:97], v[22:25]
	s_waitcnt vmcnt(4)
	v_mfma_f32_16x16x32_bf16 v[14:17], v[26:29], v[90:93], v[14:17]
	v_mfma_f32_16x16x32_bf16 v[10:13], v[26:29], v[94:97], v[10:13]
	s_waitcnt vmcnt(2)
	v_mfma_f32_16x16x32_bf16 v[6:9], v[34:37], v[90:93], v[6:9]
	v_mfma_f32_16x16x32_bf16 v[2:5], v[34:37], v[94:97], v[2:5]
	v_mfma_f32_16x16x32_bf16 v[18:21], v[30:33], v[106:109], v[18:21]
	v_mfma_f32_16x16x32_bf16 v[22:25], v[30:33], v[98:101], v[22:25]
	v_mfma_f32_16x16x32_bf16 v[14:17], v[26:29], v[106:109], v[14:17]
	v_mfma_f32_16x16x32_bf16 v[10:13], v[26:29], v[98:101], v[10:13]
	v_mfma_f32_16x16x32_bf16 v[6:9], v[34:37], v[106:109], v[6:9]
	v_mfma_f32_16x16x32_bf16 v[2:5], v[34:37], v[98:101], v[2:5]
	v_mfma_f32_16x16x32_bf16 v[18:21], v[42:45], v[90:93], v[18:21]
	v_mfma_f32_16x16x32_bf16 v[22:25], v[42:45], v[94:97], v[22:25]
	s_waitcnt vmcnt(1)
	v_mfma_f32_16x16x32_bf16 v[14:17], v[46:49], v[90:93], v[14:17]
	v_mfma_f32_16x16x32_bf16 v[10:13], v[46:49], v[94:97], v[10:13]
	s_waitcnt vmcnt(0)
	v_mfma_f32_16x16x32_bf16 v[6:9], v[38:41], v[90:93], v[6:9]
	v_mfma_f32_16x16x32_bf16 v[2:5], v[38:41], v[94:97], v[2:5]
	s_cmpk_eq_i32 s0, 0x180
	s_cbranch_scc1 .Lrt_skip1
	s_cmpk_lg_i32 s0, 0x180
	s_cselect_b32 s24, s1, 0x1200
	s_lshl_b64 s[8:9], s[24:25], 1
	v_lshl_add_u64 v[34:35], v[130:131], 0, s[8:9]
	v_lshl_add_u64 v[36:37], v[132:133], 0, s[8:9]
	s_add_i32 s8, s24, 0x200
	s_mov_b32 s9, s25
	s_addk_i32 s24, 0x400
	v_lshl_add_u64 v[38:39], s[8:9], 1, v[132:133]
	v_lshl_add_u64 v[40:41], s[24:25], 1, v[132:133]
	global_load_dwordx4 v[30:33], v[34:35], off
	global_load_dwordx4 v[26:29], v[34:35], off offset:1024
	global_load_dwordx4 v[42:45], v[36:37], off
	s_nop 0
	global_load_dwordx4 v[34:37], v[34:35], off offset:2048
	s_nop 0
	global_load_dwordx4 v[46:49], v[38:39], off
	s_nop 0
	global_load_dwordx4 v[38:41], v[40:41], off
.Lrt_skip1:
	v_permlane16_swap_b32_e32 v122, v123
	v_permlane16_swap_b32_e32 v104, v105
	global_store_dwordx2 v[58:59], v[122:123], off
	global_store_dwordx2 v[60:61], v[104:105], off
	s_addk_i32 s1, 0x600
	s_addk_i32 s0, 0x80
	v_add_u32_e32 v62, 0x8000, v62
	v_lshl_add_u64 v[58:59], v[58:59], 0, 32
	s_cmpk_lg_i32 s0, 0x200
	v_lshl_add_u64 v[60:61], v[60:61], 0, 32
	s_cbranch_scc1 .LBB0_603

; #define MX(a_, b_, c_) __builtin_amdgcn_mfma_scale_f32_16x16x128_f8f6f4(a_, b_, c_, 0, 0, 0, 0x7f7f7f7f, 0, 0x7f7f7f7f)
; #define LD32(p_) CAT8(*(const i32x4v*)(p_), *(const i32x4v*)((p_) + 16))
; #define AFRAG(mi_, ks_) CAT8(*(const i32x4v*)(smem + aoff + (mi_) * 16384 + (((8 * (ks_) + 2 * g) ^ lr) << 4)), *(const i32x4v*)(smem + aoff + (mi_) * 16384 + (((8 * (ks_) + 2 * g + 1) ^ lr) << 4)))
; #define AFRAG(hb_, mi_, ks_) CAT8(*(const i32x4v*)((hb_) + aoff + (mi_) * 4096 + (((8 * (ks_) + 2 * g2) ^ lr2) << 4)), *(const i32x4v*)((hb_) + aoff + (mi_) * 4096 + (((8 * (ks_) + 2 * g2 + 1) ^ lr2) << 4)))
; DEVINL void phase5(const Params& P, unsigned char* smem) {
;     ...
;                 for (int sk = 0; sk < 4; ++sk) {
;                     const int sn = 4 * ph + sk + 1 < 8 ? 4 * ph + sk + 1 : 7, sxn = (sn >> 1) & 1;
;                     const unsigned char* wn = wd0 + (size_t)(sxn ? e_hi : e_lo) * (2 * 64 * 2048) + (size_t)((sn & 1) * 64 + 4 * (sn >> 2)) * 2048;
;                     const unsigned char* hb = hs0 + (sk >> 1) * 20480;
;                     i32x8 fa[5];
; #pragma unroll
;                     for (int mi_ = 0; mi_ < 5; ++mi_) fa[mi_] = AFRAG(hb, mi_, sk & 1);
; #pragma unroll
;                     for (int j_ = 0; j_ < 4; ++j_) {
; #pragma unroll
;                         for (int mi_ = 0; mi_ < 5; ++mi_) acc[j_][mi_] = MX(b0[j_], fa[mi_], acc[j_][mi_]);
;                         b0[j_] = LD32(wn + j_ * 2048 + voff2);
;                         __builtin_amdgcn_sched_barrier(0);
;                     }
.LBB0_727:
	s_min_u32 s29, s28, 2
	s_add_i32 s29, s29, 5
	s_bitcmp0_b32 s29, 1
	s_cselect_b32 s30, s49, s0
	s_lshr_b32 s31, s28, 1
	s_mulk_i32 s31, 0x5000
	s_and_b32 s34, s1, 8
	v_add_u32_e32 v199, s31, v196
	s_lshl_b32 s29, s29, 17
	s_ashr_i32 s31, s30, 31
	v_add_u32_e32 v198, s34, v197
	s_and_b32 s29, s29, 0x20000
	s_lshl_b64 s[30:31], s[30:31], 18
	v_xor_b32_e32 v200, v198, v225
	v_bitop3_b32 v198, v198, v225, 1 bitop3:0x36
	s_add_u32 s30, s39, s30
	v_lshl_add_u32 v214, v200, 4, v199
	v_lshl_add_u32 v215, v198, 4, v199
	s_addc_u32 s31, s40, s31
	ds_read_b128 v[202:205], v215
	ds_read_b128 v[198:201], v214
	ds_read_b128 v[206:209], v214 offset:4096
	ds_read_b128 v[226:229], v214 offset:16384
	ds_read_b128 v[210:213], v215 offset:4096
	ds_read_b128 v[238:241], v215 offset:8192
	ds_read_b128 v[234:237], v214 offset:8192
	ds_read_b128 v[242:245], v214 offset:12288
	ds_read_b128 v[246:249], v215 offset:12288
	ds_read_b128 v[230:233], v215 offset:16384
	s_add_u32 s30, s30, s29
	s_addc_u32 s31, s31, 0
	v_lshl_add_u64 v[214:215], s[30:31], 0, v[194:195]
	v_add_co_u32_e32 v218, vcc, s47, v214
	s_waitcnt vmcnt(6) lgkmcnt(8)
	v_mfma_scale_f32_16x16x128_f8f6f4 v[190:193], v[2:9], v[198:205], v[190:193], v220, v220 op_sel_hi:[0,0,0]
	v_addc_co_u32_e32 v219, vcc, 0, v215, vcc
	v_lshl_add_u64 v[216:217], v[214:215], 0, s[20:21]
	s_waitcnt lgkmcnt(5)
	v_mfma_scale_f32_16x16x128_f8f6f4 v[186:189], v[2:9], v[206:213], v[186:189], v220, v220 op_sel_hi:[0,0,0]
	s_waitcnt lgkmcnt(3)
	v_mfma_scale_f32_16x16x128_f8f6f4 v[182:185], v[2:9], v[234:241], v[182:185], v220, v220 op_sel_hi:[0,0,0]
	s_waitcnt lgkmcnt(1)
	v_mfma_scale_f32_16x16x128_f8f6f4 v[178:181], v[2:9], v[242:249], v[178:181], v220, v220 op_sel_hi:[0,0,0]
	s_waitcnt lgkmcnt(0)
	v_mfma_scale_f32_16x16x128_f8f6f4 v[174:177], v[2:9], v[226:233], v[174:177], v220, v220 op_sel_hi:[0,0,0]
	global_load_dwordx4 v[2:5], v[218:219], off offset:-4096
	global_load_dwordx4 v[6:9], v[216:217], off offset:16
	s_waitcnt vmcnt(6)
	v_mfma_scale_f32_16x16x128_f8f6f4 v[170:173], v[10:17], v[198:205], v[170:173], v220, v220 op_sel_hi:[0,0,0]
	v_mfma_scale_f32_16x16x128_f8f6f4 v[166:169], v[10:17], v[206:213], v[166:169], v220, v220 op_sel_hi:[0,0,0]
	v_mfma_scale_f32_16x16x128_f8f6f4 v[162:165], v[10:17], v[234:241], v[162:165], v220, v220 op_sel_hi:[0,0,0]
	v_mfma_scale_f32_16x16x128_f8f6f4 v[158:161], v[10:17], v[242:249], v[158:161], v220, v220 op_sel_hi:[0,0,0]
	v_mfma_scale_f32_16x16x128_f8f6f4 v[154:157], v[10:17], v[226:233], v[154:157], v220, v220 op_sel_hi:[0,0,0]
	global_load_dwordx4 v[10:13], v[216:217], off offset:2048
	global_load_dwordx4 v[14:17], v[216:217], off offset:2064
	s_waitcnt vmcnt(6)
	v_mfma_scale_f32_16x16x128_f8f6f4 v[150:153], v[18:25], v[198:205], v[150:153], v220, v220 op_sel_hi:[0,0,0]
	v_lshl_add_u64 v[216:217], v[214:215], 0, s[22:23]
	v_mfma_scale_f32_16x16x128_f8f6f4 v[146:149], v[18:25], v[206:213], v[146:149], v220, v220 op_sel_hi:[0,0,0]
	v_mfma_scale_f32_16x16x128_f8f6f4 v[142:145], v[18:25], v[234:241], v[142:145], v220, v220 op_sel_hi:[0,0,0]
	v_mfma_scale_f32_16x16x128_f8f6f4 v[138:141], v[18:25], v[242:249], v[138:141], v220, v220 op_sel_hi:[0,0,0]
	v_mfma_scale_f32_16x16x128_f8f6f4 v[134:137], v[18:25], v[226:233], v[134:137], v220, v220 op_sel_hi:[0,0,0]
	global_load_dwordx4 v[18:21], v[218:219], off
	global_load_dwordx4 v[22:25], v[216:217], off offset:16
	s_waitcnt vmcnt(6)
	v_mfma_scale_f32_16x16x128_f8f6f4 v[130:133], v[26:33], v[198:205], v[130:133], v220, v220 op_sel_hi:[0,0,0]
	v_lshl_add_u64 v[198:199], v[214:215], 0, s[24:25]
	v_mfma_scale_f32_16x16x128_f8f6f4 v[126:129], v[26:33], v[206:213], v[126:129], v220, v220 op_sel_hi:[0,0,0]
	v_mfma_scale_f32_16x16x128_f8f6f4 v[122:125], v[26:33], v[234:241], v[122:125], v220, v220 op_sel_hi:[0,0,0]
	v_mfma_scale_f32_16x16x128_f8f6f4 v[118:121], v[26:33], v[242:249], v[118:121], v220, v220 op_sel_hi:[0,0,0]
	v_mfma_scale_f32_16x16x128_f8f6f4 v[114:117], v[26:33], v[226:233], v[114:117], v220, v220 op_sel_hi:[0,0,0]
	global_load_dwordx4 v[26:29], v[218:219], off offset:2048
	global_load_dwordx4 v[30:33], v[198:199], off offset:16
	s_add_i32 s28, s28, 1
	s_add_i32 s1, s1, 8
	s_cmp_lg_u32 s28, 3
	s_cbranch_scc1 .LBB0_727
	s_min_u32 s29, s28, 2
	s_add_i32 s29, s29, 5
	s_bitcmp0_b32 s29, 1
	s_cselect_b32 s30, s49, s0
	s_lshr_b32 s31, s28, 1
	s_mulk_i32 s31, 0x5000
	s_and_b32 s34, s1, 8
	v_add_u32_e32 v199, s31, v196
	s_lshl_b32 s29, s29, 17
	s_ashr_i32 s31, s30, 31
	v_add_u32_e32 v198, s34, v197
	s_and_b32 s29, s29, 0x20000
	s_lshl_b64 s[30:31], s[30:31], 18
	v_xor_b32_e32 v200, v198, v225
	v_bitop3_b32 v198, v198, v225, 1 bitop3:0x36
	s_add_u32 s30, s39, s30
	v_lshl_add_u32 v214, v200, 4, v199
	v_lshl_add_u32 v215, v198, 4, v199
	s_addc_u32 s31, s40, s31
	ds_read_b128 v[202:205], v215
	ds_read_b128 v[198:201], v214
	ds_read_b128 v[206:209], v214 offset:4096
	ds_read_b128 v[226:229], v214 offset:16384
	ds_read_b128 v[210:213], v215 offset:4096
	ds_read_b128 v[238:241], v215 offset:8192
	ds_read_b128 v[234:237], v214 offset:8192
	ds_read_b128 v[242:245], v214 offset:12288
	ds_read_b128 v[246:249], v215 offset:12288
	ds_read_b128 v[230:233], v215 offset:16384
	s_add_u32 s30, s30, s29
	s_addc_u32 s31, s31, 0
	v_lshl_add_u64 v[214:215], s[30:31], 0, v[194:195]
	v_add_co_u32_e32 v218, vcc, s47, v214
	s_waitcnt vmcnt(6) lgkmcnt(8)
	v_mfma_scale_f32_16x16x128_f8f6f4 v[190:193], v[2:9], v[198:205], v[190:193], v220, v220 op_sel_hi:[0,0,0]
	v_addc_co_u32_e32 v219, vcc, 0, v215, vcc
	v_lshl_add_u64 v[216:217], v[214:215], 0, s[20:21]
	s_waitcnt lgkmcnt(5)
	v_mfma_scale_f32_16x16x128_f8f6f4 v[186:189], v[2:9], v[206:213], v[186:189], v220, v220 op_sel_hi:[0,0,0]
	s_waitcnt lgkmcnt(3)
; DEVINL unsigned pk2(float lo, float hi) { const f32x2 v = {lo, hi}; return __builtin_bit_cast(unsigned, __builtin_convertvector(v, bf16v2)); }
; #define MX(a_, b_, c_) __builtin_amdgcn_mfma_scale_f32_16x16x128_f8f6f4(a_, b_, c_, 0, 0, 0, 0x7f7f7f7f, 0, 0x7f7f7f7f)
; #define LD32(p_) CAT8(*(const i32x4v*)(p_), *(const i32x4v*)((p_) + 16))
; DEVINL void phase5(const Params& P, unsigned char* smem) {
;     ...
;                         for (int mi_ = 0; mi_ < 5; ++mi_) acc[j_][mi_] = MX(b0[j_], fa[mi_], acc[j_][mi_]);
;                         b0[j_] = LD32(wn + j_ * 2048 + voff2);
;                         __builtin_amdgcn_sched_barrier(0);
;                     }
;                 }
; #pragma unroll
;                 for (int i = 0; i < 4; ++i)
; #pragma unroll
;                     for (int mi = 0; mi < 5; ++mi) {
;                         const f32x4 v = acc[i][mi] * (1.f / 128.f);
;                         q[mi] += v.x * v.x + v.y * v.y + v.z * v.z + v.w * v.w;
;                         if (ph == 0) { ypk[i][mi].x = pk2(v.x, v.y); ypk[i][mi].y = pk2(v.z, v.w); } else acc[i][mi] = v;
;                     }
	v_mfma_scale_f32_16x16x128_f8f6f4 v[182:185], v[2:9], v[234:241], v[182:185], v220, v220 op_sel_hi:[0,0,0]
	s_waitcnt lgkmcnt(1)
	v_mfma_scale_f32_16x16x128_f8f6f4 v[178:181], v[2:9], v[242:249], v[178:181], v220, v220 op_sel_hi:[0,0,0]
	s_waitcnt lgkmcnt(0)
	v_mfma_scale_f32_16x16x128_f8f6f4 v[174:177], v[2:9], v[226:233], v[174:177], v220, v220 op_sel_hi:[0,0,0]
	s_waitcnt vmcnt(4)
	v_mfma_scale_f32_16x16x128_f8f6f4 v[170:173], v[10:17], v[198:205], v[170:173], v220, v220 op_sel_hi:[0,0,0]
	v_mfma_scale_f32_16x16x128_f8f6f4 v[166:169], v[10:17], v[206:213], v[166:169], v220, v220 op_sel_hi:[0,0,0]
	v_mfma_scale_f32_16x16x128_f8f6f4 v[162:165], v[10:17], v[234:241], v[162:165], v220, v220 op_sel_hi:[0,0,0]
	v_mfma_scale_f32_16x16x128_f8f6f4 v[158:161], v[10:17], v[242:249], v[158:161], v220, v220 op_sel_hi:[0,0,0]
	v_mfma_scale_f32_16x16x128_f8f6f4 v[154:157], v[10:17], v[226:233], v[154:157], v220, v220 op_sel_hi:[0,0,0]
	s_waitcnt vmcnt(2)
	v_mfma_scale_f32_16x16x128_f8f6f4 v[150:153], v[18:25], v[198:205], v[150:153], v220, v220 op_sel_hi:[0,0,0]
	v_lshl_add_u64 v[216:217], v[214:215], 0, s[22:23]
	v_mfma_scale_f32_16x16x128_f8f6f4 v[146:149], v[18:25], v[206:213], v[146:149], v220, v220 op_sel_hi:[0,0,0]
	v_mfma_scale_f32_16x16x128_f8f6f4 v[142:145], v[18:25], v[234:241], v[142:145], v220, v220 op_sel_hi:[0,0,0]
	v_mfma_scale_f32_16x16x128_f8f6f4 v[138:141], v[18:25], v[242:249], v[138:141], v220, v220 op_sel_hi:[0,0,0]
	v_mfma_scale_f32_16x16x128_f8f6f4 v[134:137], v[18:25], v[226:233], v[134:137], v220, v220 op_sel_hi:[0,0,0]
	s_waitcnt vmcnt(0)
	v_mfma_scale_f32_16x16x128_f8f6f4 v[130:133], v[26:33], v[198:205], v[130:133], v220, v220 op_sel_hi:[0,0,0]
	v_lshl_add_u64 v[198:199], v[214:215], 0, s[24:25]
	v_mfma_scale_f32_16x16x128_f8f6f4 v[126:129], v[26:33], v[206:213], v[126:129], v220, v220 op_sel_hi:[0,0,0]
	v_mfma_scale_f32_16x16x128_f8f6f4 v[122:125], v[26:33], v[234:241], v[122:125], v220, v220 op_sel_hi:[0,0,0]
	v_mfma_scale_f32_16x16x128_f8f6f4 v[118:121], v[26:33], v[242:249], v[118:121], v220, v220 op_sel_hi:[0,0,0]
	v_mfma_scale_f32_16x16x128_f8f6f4 v[114:117], v[26:33], v[226:233], v[114:117], v220, v220 op_sel_hi:[0,0,0]
	v_pk_mul_f32 v[206:207], v[110:111], s[26:27] op_sel_hi:[1,0]
	v_pk_mul_f32 v[210:211], v[90:91], s[26:27] op_sel_hi:[1,0]
	s_waitcnt vmcnt(5)
	v_mul_f32_e32 v10, v207, v207
	s_waitcnt vmcnt(4)
	v_mul_f32_e32 v17, v211, v211
	v_pk_mul_f32 v[204:205], v[112:113], s[26:27] op_sel_hi:[1,0]
	v_pk_mul_f32 v[208:209], v[92:93], s[26:27] op_sel_hi:[1,0]
	v_fmac_f32_e32 v17, v210, v210
	v_pk_mul_f32 v[214:215], v[70:71], s[26:27] op_sel_hi:[1,0]
	v_fmac_f32_e32 v10, v206, v206
	v_fmac_f32_e32 v17, v208, v208
	s_waitcnt vmcnt(1)
	v_mul_f32_e32 v28, v215, v215
	v_pk_mul_f32 v[218:219], v[50:51], s[26:27] op_sel_hi:[1,0]
	v_fmac_f32_e32 v10, v204, v204
	v_fmac_f32_e32 v17, v209, v209
	v_pk_mul_f32 v[212:213], v[72:73], s[26:27] op_sel_hi:[1,0]
	v_fmac_f32_e32 v28, v214, v214
	s_waitcnt vmcnt(0)
	v_mul_f32_e32 v33, v219, v219
	v_fmac_f32_e32 v10, v205, v205
	v_pk_mul_f32 v[190:191], v[190:191], s[26:27] op_sel_hi:[1,0]
	v_pk_mul_f32 v[106:107], v[106:107], s[26:27] op_sel_hi:[1,0]
	v_pk_mul_f32 v[2:3], v[96:97], s[26:27] op_sel_hi:[1,0]
	v_pk_mul_f32 v[96:97], v[86:87], s[26:27] op_sel_hi:[1,0]
	v_fmac_f32_e32 v28, v212, v212
	v_pk_mul_f32 v[216:217], v[52:53], s[26:27] op_sel_hi:[1,0]
	v_fmac_f32_e32 v33, v218, v218
	v_add_f32_e32 v10, v10, v17
	v_mul_f32_e32 v17, v191, v191
	v_mul_f32_e32 v11, v107, v107
	v_mul_f32_e32 v18, v97, v97
	v_fmac_f32_e32 v28, v213, v213
	v_pk_mul_f32 v[198:199], v[66:67], s[26:27] op_sel_hi:[1,0]
	v_fmac_f32_e32 v33, v216, v216
	v_pk_mul_f32 v[192:193], v[192:193], s[26:27] op_sel_hi:[1,0]
	v_fmac_f32_e32 v17, v190, v190
	v_pk_mul_f32 v[108:109], v[108:109], s[26:27] op_sel_hi:[1,0]
	v_pk_mul_f32 v[4:5], v[94:95], s[26:27] op_sel_hi:[1,0]
	v_pk_mul_f32 v[94:95], v[88:89], s[26:27] op_sel_hi:[1,0]
	v_fmac_f32_e32 v18, v96, v96
	v_mul_f32_e32 v29, v199, v199
	v_fmac_f32_e32 v33, v217, v217
	v_pk_mul_f32 v[202:203], v[46:47], s[26:27] op_sel_hi:[1,0]
	v_fmac_f32_e32 v11, v106, v106
	v_add_f32_e32 v10, v10, v28
	v_fmac_f32_e32 v17, v192, v192
	v_fmac_f32_e32 v18, v94, v94
	v_pk_mul_f32 v[196:197], v[68:69], s[26:27] op_sel_hi:[1,0]
	v_fmac_f32_e32 v29, v198, v198
	v_mul_f32_e32 v46, v203, v203
	v_fmac_f32_e32 v11, v108, v108
	v_add_f32_e32 v10, v10, v33
	v_fmac_f32_e32 v17, v193, v193
	v_pk_mul_f32 v[112:113], v[186:187], s[26:27] op_sel_hi:[1,0]
	v_pk_mul_f32 v[102:103], v[102:103], s[26:27] op_sel_hi:[1,0]
	v_fmac_f32_e32 v18, v95, v95
	v_pk_mul_f32 v[82:83], v[82:83], s[26:27] op_sel_hi:[1,0]
	v_fmac_f32_e32 v29, v196, v196
	v_pk_mul_f32 v[200:201], v[48:49], s[26:27] op_sel_hi:[1,0]
	v_fmac_f32_e32 v46, v202, v202
	v_fmac_f32_e32 v11, v109, v109
	v_add_f32_e32 v17, v10, v17
	v_mul_f32_e32 v10, v113, v113
	v_mul_f32_e32 v12, v103, v103
	v_mul_f32_e32 v19, v83, v83
	v_fmac_f32_e32 v29, v197, v197
	v_pk_mul_f32 v[70:71], v[62:63], s[26:27] op_sel_hi:[1,0]
	v_fmac_f32_e32 v46, v200, v200
	v_add_f32_e32 v11, v11, v18
	v_pk_mul_f32 v[110:111], v[188:189], s[26:27] op_sel_hi:[1,0]
	v_fmac_f32_e32 v10, v112, v112
	v_pk_mul_f32 v[104:105], v[104:105], s[26:27] op_sel_hi:[1,0]
	v_pk_mul_f32 v[84:85], v[84:85], s[26:27] op_sel_hi:[1,0]
	v_fmac_f32_e32 v19, v82, v82
	v_pk_mul_f32 v[8:9], v[74:75], s[26:27] op_sel_hi:[1,0]
	v_mul_f32_e32 v30, v71, v71
	v_fmac_f32_e32 v46, v201, v201
	v_pk_mul_f32 v[74:75], v[42:43], s[26:27] op_sel_hi:[1,0]
	v_fmac_f32_e32 v12, v102, v102
	v_add_f32_e32 v11, v11, v29
	v_fmac_f32_e32 v10, v110, v110
	v_mul_f32_e32 v16, v5, v5
	v_fmac_f32_e32 v19, v84, v84
; DEVINL unsigned pk2(float lo, float hi) { const f32x2 v = {lo, hi}; return __builtin_bit_cast(unsigned, __builtin_convertvector(v, bf16v2)); }
; DEVINL void phase5(const Params& P, unsigned char* smem) {
;     ...
; #pragma unroll
;                 for (int i = 0; i < 4; ++i)
; #pragma unroll
;                     for (int mi = 0; mi < 5; ++mi) {
;                         const f32x4 v = acc[i][mi] * (1.f / 128.f);
;                         q[mi] += v.x * v.x + v.y * v.y + v.z * v.z + v.w * v.w;
;                         if (ph == 0) { ypk[i][mi].x = pk2(v.x, v.y); ypk[i][mi].y = pk2(v.z, v.w); } else acc[i][mi] = v;
;                     }
	v_mul_f32_e32 v27, v9, v9
	v_pk_mul_f32 v[64:65], v[64:65], s[26:27] op_sel_hi:[1,0]
	v_fmac_f32_e32 v30, v70, v70
	v_pk_mul_f32 v[20:21], v[54:55], s[26:27] op_sel_hi:[1,0]
	v_mul_f32_e32 v47, v75, v75
	v_fmac_f32_e32 v12, v104, v104
	v_add_f32_e32 v11, v11, v46
	v_fmac_f32_e32 v10, v111, v111
	v_pk_mul_f32 v[62:63], v[182:183], s[26:27] op_sel_hi:[1,0]
	v_pk_mul_f32 v[98:99], v[98:99], s[26:27] op_sel_hi:[1,0]
	v_fmac_f32_e32 v19, v85, v85
	v_pk_mul_f32 v[78:79], v[78:79], s[26:27] op_sel_hi:[1,0]
	v_pk_mul_f32 v[6:7], v[76:77], s[26:27] op_sel_hi:[1,0]
	v_fmac_f32_e32 v27, v8, v8
	v_fmac_f32_e32 v30, v64, v64
	v_mul_f32_e32 v32, v21, v21
	v_pk_mul_f32 v[72:73], v[44:45], s[26:27] op_sel_hi:[1,0]
	v_fmac_f32_e32 v47, v74, v74
	v_pk_mul_f32 v[24:25], v[34:35], s[26:27] op_sel_hi:[1,0]
	v_fmac_f32_e32 v12, v105, v105
	v_fmac_f32_e32 v16, v4, v4
	v_add_f32_e32 v18, v11, v10
	v_mul_f32_e32 v10, v63, v63
	v_mul_f32_e32 v13, v99, v99
	v_mul_f32_e32 v26, v79, v79
	v_fmac_f32_e32 v27, v6, v6
	v_fmac_f32_e32 v30, v65, v65
	v_pk_mul_f32 v[58:59], v[58:59], s[26:27] op_sel_hi:[1,0]
	v_pk_mul_f32 v[14:15], v[56:57], s[26:27] op_sel_hi:[1,0]
	v_fmac_f32_e32 v32, v20, v20
	v_fmac_f32_e32 v47, v72, v72
	v_mul_f32_e32 v34, v25, v25
	v_fmac_f32_e32 v16, v2, v2
	v_add_f32_e32 v12, v12, v19
	v_pk_mul_f32 v[56:57], v[184:185], s[26:27] op_sel_hi:[1,0]
	v_fmac_f32_e32 v10, v62, v62
	v_pk_mul_f32 v[100:101], v[100:101], s[26:27] op_sel_hi:[1,0]
	v_pk_mul_f32 v[80:81], v[80:81], s[26:27] op_sel_hi:[1,0]
	v_fmac_f32_e32 v26, v78, v78
	v_fmac_f32_e32 v27, v7, v7
	v_mul_f32_e32 v31, v59, v59
	v_fmac_f32_e32 v32, v14, v14
	v_fmac_f32_e32 v47, v73, v73
	v_pk_mul_f32 v[44:45], v[38:39], s[26:27] op_sel_hi:[1,0]
	v_pk_mul_f32 v[22:23], v[36:37], s[26:27] op_sel_hi:[1,0]
	v_fmac_f32_e32 v34, v24, v24
	v_fmac_f32_e32 v13, v98, v98
	v_fmac_f32_e32 v16, v3, v3
	v_add_f32_e32 v12, v12, v30
	v_fmac_f32_e32 v10, v56, v56
	v_fmac_f32_e32 v26, v80, v80
	v_pk_mul_f32 v[60:61], v[60:61], s[26:27] op_sel_hi:[1,0]
	v_fmac_f32_e32 v31, v58, v58
	v_fmac_f32_e32 v32, v15, v15
	v_mul_f32_e32 v38, v45, v45
	v_fmac_f32_e32 v34, v22, v22
	v_fmac_f32_e32 v13, v100, v100
	v_add_f32_e32 v16, v16, v27
	v_add_f32_e32 v12, v12, v47
	v_fmac_f32_e32 v10, v57, v57
	v_pk_mul_f32 v[36:37], v[178:179], s[26:27] op_sel_hi:[1,0]
	v_fmac_f32_e32 v26, v81, v81
	v_fmac_f32_e32 v31, v60, v60
	v_pk_mul_f32 v[42:43], v[40:41], s[26:27] op_sel_hi:[1,0]
	v_fmac_f32_e32 v38, v44, v44
	v_fmac_f32_e32 v34, v23, v23
	v_fmac_f32_e32 v13, v101, v101
	v_add_f32_e32 v16, v16, v32
	v_add_f32_e32 v19, v12, v10
	v_mul_f32_e32 v10, v37, v37
	v_fmac_f32_e32 v31, v61, v61
	v_fmac_f32_e32 v38, v42, v42
	v_add_f32_e32 v13, v13, v26
	v_add_f32_e32 v16, v16, v34
	v_pk_mul_f32 v[34:35], v[180:181], s[26:27] op_sel_hi:[1,0]
	v_fmac_f32_e32 v10, v36, v36
	v_fmac_f32_e32 v38, v43, v43
	v_add_f32_e32 v13, v13, v31
	v_fmac_f32_e32 v10, v34, v34
	v_add_f32_e32 v13, v13, v38
	v_fmac_f32_e32 v10, v35, v35
	v_add_f32_e32 v26, v13, v10
	v_pk_mul_f32 v[12:13], v[174:175], s[26:27] op_sel_hi:[1,0]
	v_pk_mul_f32 v[10:11], v[176:177], s[26:27] op_sel_hi:[1,0]
	v_mul_f32_e32 v27, v13, v13
	v_fmac_f32_e32 v27, v12, v12
	v_fmac_f32_e32 v27, v10, v10
	v_fmac_f32_e32 v27, v11, v11
	v_pk_mul_f32 v[170:171], v[170:171], s[26:27] op_sel_hi:[1,0]
	v_add_f32_e32 v27, v16, v27
	v_mul_f32_e32 v16, v171, v171
	v_pk_mul_f32 v[172:173], v[172:173], s[26:27] op_sel_hi:[1,0]
	v_fmac_f32_e32 v16, v170, v170
	v_fmac_f32_e32 v16, v172, v172
	v_fmac_f32_e32 v16, v173, v173
	v_pk_mul_f32 v[166:167], v[166:167], s[26:27] op_sel_hi:[1,0]
	v_add_f32_e32 v28, v17, v16
	v_mul_f32_e32 v16, v167, v167
	v_pk_mul_f32 v[168:169], v[168:169], s[26:27] op_sel_hi:[1,0]
	v_fmac_f32_e32 v16, v166, v166
	v_fmac_f32_e32 v16, v168, v168
	v_fmac_f32_e32 v16, v169, v169
	v_pk_mul_f32 v[68:69], v[162:163], s[26:27] op_sel_hi:[1,0]
	v_add_f32_e32 v29, v18, v16
	v_mul_f32_e32 v16, v69, v69
	v_pk_mul_f32 v[66:67], v[164:165], s[26:27] op_sel_hi:[1,0]
	v_fmac_f32_e32 v16, v68, v68
	v_fmac_f32_e32 v16, v66, v66
	v_fmac_f32_e32 v16, v67, v67
	v_pk_mul_f32 v[40:41], v[158:159], s[26:27] op_sel_hi:[1,0]
	v_add_f32_e32 v30, v19, v16
	v_mul_f32_e32 v16, v41, v41
	v_pk_mul_f32 v[38:39], v[160:161], s[26:27] op_sel_hi:[1,0]
	v_fmac_f32_e32 v16, v40, v40
; DEVINL unsigned pk2(float lo, float hi) { const f32x2 v = {lo, hi}; return __builtin_bit_cast(unsigned, __builtin_convertvector(v, bf16v2)); }
; DEVINL void phase5(const Params& P, unsigned char* smem) {
;     ...
; #pragma unroll
;                 for (int i = 0; i < 4; ++i)
; #pragma unroll
;                     for (int mi = 0; mi < 5; ++mi) {
;                         const f32x4 v = acc[i][mi] * (1.f / 128.f);
;                         q[mi] += v.x * v.x + v.y * v.y + v.z * v.z + v.w * v.w;
;                         if (ph == 0) { ypk[i][mi].x = pk2(v.x, v.y); ypk[i][mi].y = pk2(v.z, v.w); } else acc[i][mi] = v;
;                     }
;             }
;     ...
; #pragma unroll
;             for (int mi = 0; mi < 5; ++mi) { q[mi] = gsum4(q[mi]); }
;             if (g2 == 0) {
; #pragma unroll
;                 for (int mi = 0; mi < 5; ++mi) s_part[wv * 80 + 16 * mi + lr2] = q[mi];
;             }
	v_fmac_f32_e32 v16, v38, v38
	v_pk_mul_f32 v[18:19], v[154:155], s[26:27] op_sel_hi:[1,0]
	v_fmac_f32_e32 v16, v39, v39
	v_mul_f32_e32 v31, v19, v19
	v_add_f32_e32 v26, v26, v16
	v_pk_mul_f32 v[16:17], v[156:157], s[26:27] op_sel_hi:[1,0]
	v_fmac_f32_e32 v31, v18, v18
	v_fmac_f32_e32 v31, v16, v16
	v_fmac_f32_e32 v31, v17, v17
	v_pk_mul_f32 v[150:151], v[150:151], s[26:27] op_sel_hi:[1,0]
	v_add_f32_e32 v31, v27, v31
	v_mul_f32_e32 v27, v151, v151
	v_pk_mul_f32 v[152:153], v[152:153], s[26:27] op_sel_hi:[1,0]
	v_fmac_f32_e32 v27, v150, v150
	v_fmac_f32_e32 v27, v152, v152
	v_fmac_f32_e32 v27, v153, v153
	v_pk_mul_f32 v[146:147], v[146:147], s[26:27] op_sel_hi:[1,0]
	v_add_f32_e32 v32, v28, v27
	v_mul_f32_e32 v27, v147, v147
	v_pk_mul_f32 v[148:149], v[148:149], s[26:27] op_sel_hi:[1,0]
	v_fmac_f32_e32 v27, v146, v146
	v_fmac_f32_e32 v27, v148, v148
	v_fmac_f32_e32 v27, v149, v149
	v_pk_mul_f32 v[86:87], v[142:143], s[26:27] op_sel_hi:[1,0]
	v_add_f32_e32 v33, v29, v27
	v_mul_f32_e32 v27, v87, v87
	v_pk_mul_f32 v[76:77], v[144:145], s[26:27] op_sel_hi:[1,0]
	v_fmac_f32_e32 v27, v86, v86
	v_fmac_f32_e32 v27, v76, v76
	v_fmac_f32_e32 v27, v77, v77
	v_pk_mul_f32 v[48:49], v[138:139], s[26:27] op_sel_hi:[1,0]
	v_add_f32_e32 v30, v30, v27
	v_mul_f32_e32 v27, v49, v49
	v_pk_mul_f32 v[46:47], v[140:141], s[26:27] op_sel_hi:[1,0]
	v_fmac_f32_e32 v27, v48, v48
	v_fmac_f32_e32 v27, v46, v46
	v_pk_mul_f32 v[28:29], v[134:135], s[26:27] op_sel_hi:[1,0]
	v_fmac_f32_e32 v27, v47, v47
	v_mul_f32_e32 v50, v29, v29
	v_add_f32_e32 v54, v26, v27
	v_pk_mul_f32 v[26:27], v[136:137], s[26:27] op_sel_hi:[1,0]
	v_fmac_f32_e32 v50, v28, v28
	v_fmac_f32_e32 v50, v26, v26
	v_fmac_f32_e32 v50, v27, v27
	v_pk_mul_f32 v[136:137], v[130:131], s[26:27] op_sel_hi:[1,0]
	v_add_f32_e32 v55, v31, v50
	v_mul_f32_e32 v31, v137, v137
	v_pk_mul_f32 v[132:133], v[132:133], s[26:27] op_sel_hi:[1,0]
	v_fmac_f32_e32 v31, v136, v136
	v_fmac_f32_e32 v31, v132, v132
	v_fmac_f32_e32 v31, v133, v133
	v_pk_mul_f32 v[126:127], v[126:127], s[26:27] op_sel_hi:[1,0]
	v_add_f32_e32 v92, v32, v31
	v_mul_f32_e32 v31, v127, v127
	v_pk_mul_f32 v[128:129], v[128:129], s[26:27] op_sel_hi:[1,0]
	v_fmac_f32_e32 v31, v126, v126
	v_fmac_f32_e32 v31, v128, v128
	v_fmac_f32_e32 v31, v129, v129
	v_pk_mul_f32 v[90:91], v[122:123], s[26:27] op_sel_hi:[1,0]
	v_add_f32_e32 v93, v33, v31
	v_mul_f32_e32 v31, v91, v91
	v_pk_mul_f32 v[88:89], v[124:125], s[26:27] op_sel_hi:[1,0]
	v_fmac_f32_e32 v31, v90, v90
	v_fmac_f32_e32 v31, v88, v88
	v_fmac_f32_e32 v31, v89, v89
	v_pk_mul_f32 v[52:53], v[118:119], s[26:27] op_sel_hi:[1,0]
	v_add_f32_e32 v122, v30, v31
	v_mul_f32_e32 v30, v53, v53
	v_pk_mul_f32 v[50:51], v[120:121], s[26:27] op_sel_hi:[1,0]
	v_fmac_f32_e32 v30, v52, v52
	v_fmac_f32_e32 v30, v50, v50
	v_fmac_f32_e32 v30, v51, v51
	v_pk_mul_f32 v[32:33], v[114:115], s[26:27] op_sel_hi:[1,0]
	v_add_f32_e32 v118, v54, v30
	v_mul_f32_e32 v54, v33, v33
	v_pk_mul_f32 v[30:31], v[116:117], s[26:27] op_sel_hi:[1,0]
	v_fmac_f32_e32 v54, v32, v32
	v_fmac_f32_e32 v54, v30, v30
	v_fmac_f32_e32 v54, v31, v31
	v_add_f32_e32 v119, v55, v54
	v_mov_b32_e32 v54, v92
	v_mov_b32_e32 v116, v118
	s_nop 0
	v_permlane16_swap_b32_e32 v92, v54
	v_permlane16_swap_b32_e32 v118, v116
	v_add_f32_e32 v54, v92, v54
	v_mov_b32_e32 v92, v93
	v_mov_b32_e32 v114, v122
	v_add_f32_e32 v116, v118, v116
	v_mov_b32_e32 v118, v119
	v_permlane16_swap_b32_e32 v93, v92
	v_permlane16_swap_b32_e32 v122, v114
	v_permlane16_swap_b32_e32 v119, v118
	v_add_f32_e32 v92, v93, v92
	v_add_f32_e32 v114, v122, v114
	v_add_f32_e32 v118, v119, v118
	v_mov_b32_e32 v55, v54
	v_mov_b32_e32 v93, v92
	v_mov_b32_e32 v115, v114
	v_mov_b32_e32 v117, v116
	v_mov_b32_e32 v119, v118
	v_permlane32_swap_b32_e32 v54, v55
	v_permlane32_swap_b32_e32 v92, v93
	v_permlane32_swap_b32_e32 v114, v115
	v_permlane32_swap_b32_e32 v116, v117
	v_permlane32_swap_b32_e32 v118, v119
	v_cmp_gt_u32_e32 vcc, 16, v223
	s_and_saveexec_b64 s[0:1], vcc
	s_cbranch_execz .LBB0_730
	v_add_f32_e32 v92, v92, v93
	v_add_f32_e32 v54, v54, v55
	v_lshl_add_u32 v55, v223, 2, s27
	v_add_f32_e32 v118, v118, v119
	v_add_f32_e32 v116, v116, v117
	v_add_f32_e32 v114, v114, v115
	ds_write2_b32 v55, v54, v92 offset1:16
	ds_write2_b32 v55, v114, v116 offset0:32 offset1:48
	ds_write_b32 v55, v118 offset:256
